# gla_out decay-gate projection: the 64 ds_read_b128 per thread (each followed by lgkmcnt(0) in the compiler's code) go through a pool of 8 free quads with counted lgkmcnt; s_nop kept where a moved read
# baseline (speedup 1.0000x reference)
.LBB0_522:
	s_mov_b32 s60, s12
	s_ashr_i32 s20, s12, 6
	s_and_b32 s12, s12, 63
	s_ashr_i32 s46, s60, 8
	s_lshl_b32 s18, s12, 6
	s_ashr_i32 s21, s20, 31
	s_lshl_b32 s12, s12, 8
	s_ashr_i32 s47, s46, 31
	s_lshl_b64 s[62:63], s[20:21], 14
	s_add_i32 s12, s12, s90
	v_mov_b32_e32 v161, v185
	s_add_u32 s12, s62, s12
	s_addc_u32 s21, s63, 0
	v_and_b32_e32 v197, 31, v161
	v_or_b32_e32 v2, s12, v197
	v_mov_b32_e32 v3, s21
	v_bfe_u32 v163, v161, 5, 1
	v_lshlrev_b64 v[2:3], 8, v[2:3]
	s_lshl_b64 s[46:47], s[46:47], 12
	v_lshl_add_u64 v[2:3], s[52:53], 0, v[2:3]
	v_lshlrev_b32_e32 v182, 4, v163
	v_mov_b32_e32 v183, v1
	s_or_b32 s46, s46, s18
	v_lshl_add_u64 v[2:3], v[2:3], 0, v[182:183]
	v_or_b32_e32 v196, s46, v197
	v_mov_b64_e32 v[180:181], s[50:51]
	s_movk_i32 s72, 0x4800
	global_load_dwordx4 v[78:81], v[2:3], off
	global_load_dwordx4 v[74:77], v[2:3], off offset:32
	global_load_dwordx4 v[70:73], v[2:3], off offset:64
	global_load_dwordx4 v[66:69], v[2:3], off offset:96
	global_load_dwordx4 v[62:65], v[2:3], off offset:128
	global_load_dwordx4 v[58:61], v[2:3], off offset:160
	global_load_dwordx4 v[54:57], v[2:3], off offset:192
	global_load_dwordx4 v[50:53], v[2:3], off offset:224
	s_and_b32 s62, s20, 3
	v_mad_u64_u32 v[2:3], s[20:21], v196, s72, v[180:181]
	v_mov_b32_e32 v4, 0x4800
	v_mad_i32_i24 v3, s47, v4, v3
	s_lshl_b32 s30, s62, 9
	s_lshl_b32 s20, s90, 1
	s_mov_b32 s21, s31
	v_lshl_add_u64 v[2:3], v[2:3], 0, s[30:31]
	v_lshlrev_b32_e32 v0, 3, v163
	v_lshl_add_u64 v[2:3], v[2:3], 0, s[20:21]
	v_lshl_add_u64 v[2:3], v[2:3], 0, v[0:1]
	s_movk_i32 s69, 0x2000
	s_mov_b64 s[20:21], 0x2800
	v_add_co_u32_e32 v6, vcc, s69, v2
	v_lshl_add_u64 v[4:5], v[2:3], 0, s[20:21]
	s_nop 0
	v_addc_co_u32_e32 v7, vcc, 0, v3, vcc
	s_mov_b64 s[20:21], 0x92800
	s_mov_b32 s12, 0x92000
	global_load_dwordx2 v[178:179], v[6:7], off offset:2048
	global_load_dwordx2 v[176:177], v[4:5], off offset:16
	global_load_dwordx2 v[174:175], v[4:5], off offset:32
	global_load_dwordx2 v[172:173], v[4:5], off offset:48
	v_lshl_add_u64 v[4:5], v[2:3], 0, s[20:21]
	v_add_co_u32_e32 v2, vcc, s12, v2
	s_movk_i32 s68, 0x1000
	s_nop 0
	v_addc_co_u32_e32 v3, vcc, 0, v3, vcc
	global_load_dwordx2 v[170:171], v[2:3], off offset:2048
	global_load_dwordx2 v[168:169], v[4:5], off offset:16
	global_load_dwordx2 v[166:167], v[4:5], off offset:32
	global_load_dwordx2 v[164:165], v[4:5], off offset:48
	v_lshl_add_u64 v[2:3], s[46:47], 0, v[146:147]
	v_lshlrev_b64 v[2:3], 7, v[2:3]
	s_barrier
	s_waitcnt vmcnt(23)
	ds_write_b128 v190, v[34:37] offset:8192
	s_waitcnt vmcnt(22)
	ds_write_b128 v190, v[38:41] offset:24576
	s_waitcnt vmcnt(21)
	ds_write_b128 v191, v[42:45] offset:8192
	s_waitcnt vmcnt(20)
	ds_write_b128 v191, v[46:49] offset:24576
	s_waitcnt vmcnt(19)
	ds_write_b128 v192, v[82:85] offset:40960
	s_waitcnt vmcnt(18)
	ds_write_b128 v193, v[86:89] offset:40960
	s_waitcnt vmcnt(17)
	ds_write_b128 v194, v[90:93] offset:40960
	s_waitcnt vmcnt(16)
	ds_write_b128 v195, v[94:97] offset:40960
	v_lshl_add_u64 v[2:3], v[158:159], 0, v[2:3]
	global_load_dword v0, v[2:3], off
	v_lshl_add_u64 v[2:3], s[46:47], 0, v[148:149]
	v_lshlrev_b64 v[2:3], 7, v[2:3]
	v_lshl_add_u64 v[2:3], v[158:159], 0, v[2:3]
	global_load_dword v2, v[2:3], off
	s_movk_i32 s12, 0x3000
	s_movk_i32 s20, 0xf0
	s_movk_i32 s18, 0x7fff
	v_bfe_u32 v208, v161, 2, 2
	v_lshl_add_u32 v201, v197, 8, 0
	v_or_b32_e32 v90, 2, v163
	v_lshlrev_b32_e32 v198, 2, v163
	v_mov_b32_e32 v183, s47
	v_cmp_lt_u32_e64 s[46:47], v198, v197
	v_and_b32_e32 v199, 63, v161
	v_readlane_b32 s64, v254, 18
	v_readlane_b32 s65, v254, 19
	v_readlane_b32 s66, v254, 20
	v_readlane_b32 s67, v254, 21
	s_waitcnt vmcnt(0)
	ds_write2st64_b32 v187, v0, v2 offset1:8
	v_lshl_or_b32 v0, v186, 2, s30
	v_lshl_add_u64 v[18:19], s[54:55], 0, v[0:1]
	v_add_co_u32_e32 v2, vcc, s68, v18
	global_load_dword v14, v0, s[54:55]
	global_load_dword v15, v0, s[54:55] offset:2048
	v_addc_co_u32_e32 v3, vcc, 0, v19, vcc
	v_add_co_u32_e32 v4, vcc, s69, v18
	s_nop 1
	v_addc_co_u32_e32 v5, vcc, 0, v19, vcc
	global_load_dword v16, v[4:5], off offset:-4096
	global_load_dword v17, v[2:3], off offset:2048
	global_load_dword v6, v[4:5], off
	global_load_dword v7, v[4:5], off offset:2048
	v_add_co_u32_e32 v2, vcc, s12, v18
	s_movk_i32 s12, 0x4000
	s_nop 0
	v_addc_co_u32_e32 v3, vcc, 0, v19, vcc
	v_add_co_u32_e32 v4, vcc, s12, v18
	s_movk_i32 s12, 0x5000
	s_nop 0
	v_addc_co_u32_e32 v5, vcc, 0, v19, vcc
	global_load_dword v10, v[4:5], off offset:-4096
	global_load_dword v11, v[2:3], off offset:2048
	global_load_dword v8, v[4:5], off
	global_load_dword v9, v[4:5], off offset:2048
	v_add_co_u32_e32 v2, vcc, s12, v18
	s_movk_i32 s12, 0x6000
	s_nop 0
	v_addc_co_u32_e32 v3, vcc, 0, v19, vcc
	v_add_co_u32_e32 v4, vcc, s12, v18
	s_movk_i32 s12, 0x7000
	s_nop 0
	v_addc_co_u32_e32 v5, vcc, 0, v19, vcc
	v_add_co_u32_e32 v18, vcc, s12, v18
	global_load_dword v12, v[4:5], off offset:-4096
	global_load_dword v13, v[2:3], off offset:2048
	s_nop 0
	global_load_dword v2, v[4:5], off
	s_nop 0
	global_load_dword v4, v[4:5], off offset:2048
	v_addc_co_u32_e32 v19, vcc, 0, v19, vcc
	global_load_dword v5, v[18:19], off
	global_load_dword v3, v[18:19], off offset:2048
	s_nop 0
	global_load_dword v18, v0, s[56:57]
	s_waitcnt lgkmcnt(0)
	s_barrier
	ds_read_b128 v[38:41], v188
	ds_read_b128 v[42:45], v188 offset:16
	ds_read_b128 v[46:49], v188 offset:32
	ds_read_b128 v[82:85], v188 offset:48
	ds_read_b128 v[86:89], v188 offset:64
	ds_read_b128 v[92:95], v188 offset:80
	ds_read_b128 v[96:99], v188 offset:96
	ds_read_b128 v[100:103], v188 offset:112
	s_mov_b32 s12, 0x3d800000
	v_cmp_gt_u32_e32 vcc, v198, v197
	s_waitcnt vmcnt(15)
	s_waitcnt lgkmcnt(7)
	v_mul_f32_e32 v0, v15, v39
	v_fmac_f32_e32 v0, v14, v38
	s_waitcnt vmcnt(14)
	v_fmac_f32_e32 v0, v16, v40
	s_waitcnt vmcnt(13)
	v_fmac_f32_e32 v0, v17, v41
	ds_read_b128 v[38:41], v188 offset:128
	s_waitcnt vmcnt(11)
	s_waitcnt lgkmcnt(7)
	v_mul_f32_e32 v19, v7, v43
	v_fmac_f32_e32 v19, v6, v42
	s_waitcnt vmcnt(10)
	v_fmac_f32_e32 v19, v10, v44
	s_waitcnt vmcnt(9)
	v_fmac_f32_e32 v19, v11, v45
	ds_read_b128 v[42:45], v188 offset:144
	s_waitcnt vmcnt(0)
	v_add_f32_e32 v0, v18, v0
	v_add_f32_e32 v0, v0, v19
	s_waitcnt lgkmcnt(7)
	v_mul_f32_e32 v19, v9, v47
	v_fmac_f32_e32 v19, v8, v46
	v_fmac_f32_e32 v19, v12, v48
	v_fmac_f32_e32 v19, v13, v49
	ds_read_b128 v[46:49], v188 offset:160
	v_add_f32_e32 v0, v0, v19
	s_waitcnt lgkmcnt(7)
	v_mul_f32_e32 v19, v4, v83
	v_fmac_f32_e32 v19, v2, v82
	v_fmac_f32_e32 v19, v5, v84
	v_fmac_f32_e32 v19, v3, v85
	ds_read_b128 v[82:85], v188 offset:176
	v_add_f32_e32 v0, v0, v19
	v_min_f32_e32 v19, 0, v0
	v_mul_f32_e64 v0, |v0|, s24
	v_exp_f32_e32 v0, v0
	s_nop 0
	v_add_f32_e32 v0, 1.0, v0
	v_log_f32_e32 v0, v0
	s_nop 0
	v_fmac_f32_e32 v19, 0xbf317218, v0
	v_fma_f32 v0, v19, s12, 0
	s_waitcnt lgkmcnt(7)
	v_mul_f32_e32 v19, v15, v87
	v_fmac_f32_e32 v19, v14, v86
	v_fmac_f32_e32 v19, v16, v88
	v_fmac_f32_e32 v19, v17, v89
	ds_read_b128 v[86:89], v188 offset:192
	v_add_f32_e32 v19, v18, v19
	s_movk_i32 s12, 0x80
	s_waitcnt lgkmcnt(7)
	v_mul_f32_e32 v21, v7, v93
	v_fmac_f32_e32 v21, v6, v92
	v_fmac_f32_e32 v21, v10, v94
	v_fmac_f32_e32 v21, v11, v95
	ds_read_b128 v[92:95], v188 offset:208
	v_add_f32_e32 v19, v19, v21
	s_waitcnt lgkmcnt(7)
	v_mul_f32_e32 v21, v9, v97
	v_fmac_f32_e32 v21, v8, v96
	v_fmac_f32_e32 v21, v12, v98
	v_fmac_f32_e32 v21, v13, v99
	ds_read_b128 v[96:99], v188 offset:224
	v_add_f32_e32 v19, v19, v21
	s_waitcnt lgkmcnt(7)
	v_mul_f32_e32 v21, v4, v101
	v_fmac_f32_e32 v21, v2, v100
	v_fmac_f32_e32 v21, v5, v102
	v_fmac_f32_e32 v21, v3, v103
	ds_read_b128 v[100:103], v188 offset:240
	v_add_f32_e32 v19, v19, v21
	v_min_f32_e32 v20, 0, v19
	v_mul_f32_e64 v19, |v19|, s24
	v_exp_f32_e32 v19, v19
	s_nop 0
	v_add_f32_e32 v19, 1.0, v19
	v_log_f32_e32 v19, v19
	s_nop 0
	v_fmac_f32_e32 v20, 0xbf317218, v19
	v_fmamk_f32 v19, v20, 0x3d800000, v0
	s_waitcnt lgkmcnt(7)
	v_mul_f32_e32 v21, v15, v39
	v_fmac_f32_e32 v21, v14, v38
	v_fmac_f32_e32 v21, v16, v40
	v_fmac_f32_e32 v21, v17, v41
	ds_read_b128 v[38:41], v188 offset:256
	v_add_f32_e32 v24, v18, v21
	s_waitcnt lgkmcnt(7)
	v_mul_f32_e32 v21, v7, v43
	v_fmac_f32_e32 v21, v6, v42
	v_fmac_f32_e32 v21, v10, v44
	v_fmac_f32_e32 v21, v11, v45
	ds_read_b128 v[42:45], v188 offset:272
	v_add_f32_e32 v24, v24, v21
	s_waitcnt lgkmcnt(7)
	v_mul_f32_e32 v21, v9, v47
	v_fmac_f32_e32 v21, v8, v46
	v_fmac_f32_e32 v21, v12, v48
	v_fmac_f32_e32 v21, v13, v49
	ds_read_b128 v[46:49], v188 offset:288
	v_add_f32_e32 v24, v24, v21
	s_waitcnt lgkmcnt(7)
	v_mul_f32_e32 v21, v4, v83
	v_fmac_f32_e32 v21, v2, v82
	v_fmac_f32_e32 v21, v5, v84
	v_fmac_f32_e32 v21, v3, v85
	ds_read_b128 v[82:85], v188 offset:304
	v_add_f32_e32 v20, v24, v21
	v_min_f32_e32 v21, 0, v20
	v_mul_f32_e64 v20, |v20|, s24
	v_exp_f32_e32 v20, v20
	s_nop 0
	v_add_f32_e32 v20, 1.0, v20
	v_log_f32_e32 v20, v20
	s_nop 0
	v_fmac_f32_e32 v21, 0xbf317218, v20
	v_fmamk_f32 v20, v21, 0x3d800000, v19
	s_waitcnt lgkmcnt(7)
	v_mul_f32_e32 v21, v15, v87
	v_fmac_f32_e32 v21, v14, v86
	v_fmac_f32_e32 v21, v16, v88
	v_fmac_f32_e32 v21, v17, v89
	ds_read_b128 v[86:89], v188 offset:320
	v_add_f32_e32 v21, v18, v21
	s_waitcnt lgkmcnt(7)
	v_mul_f32_e32 v23, v7, v93
	v_fmac_f32_e32 v23, v6, v92
	v_fmac_f32_e32 v23, v10, v94
	v_fmac_f32_e32 v23, v11, v95
	ds_read_b128 v[92:95], v188 offset:336
	v_add_f32_e32 v21, v21, v23
	s_waitcnt lgkmcnt(7)
	v_mul_f32_e32 v23, v9, v97
	v_fmac_f32_e32 v23, v8, v96
	v_fmac_f32_e32 v23, v12, v98
	v_fmac_f32_e32 v23, v13, v99
	ds_read_b128 v[96:99], v188 offset:352
	v_add_f32_e32 v21, v21, v23
	s_waitcnt lgkmcnt(7)
	v_mul_f32_e32 v23, v4, v101
	v_fmac_f32_e32 v23, v2, v100
	v_fmac_f32_e32 v23, v5, v102
	v_fmac_f32_e32 v23, v3, v103
	ds_read_b128 v[100:103], v188 offset:368
	v_add_f32_e32 v21, v21, v23
	v_min_f32_e32 v22, 0, v21
	v_mul_f32_e64 v21, |v21|, s24
	v_exp_f32_e32 v21, v21
	s_nop 0
	v_add_f32_e32 v21, 1.0, v21
	v_log_f32_e32 v21, v21
	s_nop 0
	v_fmac_f32_e32 v22, 0xbf317218, v21
	v_fmamk_f32 v21, v22, 0x3d800000, v20
	s_waitcnt lgkmcnt(7)
	v_mul_f32_e32 v23, v15, v39
	v_fmac_f32_e32 v23, v14, v38
	v_fmac_f32_e32 v23, v16, v40
	v_fmac_f32_e32 v23, v17, v41
	ds_read_b128 v[38:41], v188 offset:384
	v_add_f32_e32 v26, v18, v23
	s_waitcnt lgkmcnt(7)
	v_mul_f32_e32 v23, v7, v43
	v_fmac_f32_e32 v23, v6, v42
	v_fmac_f32_e32 v23, v10, v44
	v_fmac_f32_e32 v23, v11, v45
	ds_read_b128 v[42:45], v188 offset:400
	v_add_f32_e32 v26, v26, v23
	s_waitcnt lgkmcnt(7)
	v_mul_f32_e32 v23, v9, v47
	v_fmac_f32_e32 v23, v8, v46
	v_fmac_f32_e32 v23, v12, v48
	v_fmac_f32_e32 v23, v13, v49
	ds_read_b128 v[46:49], v188 offset:416
	v_add_f32_e32 v26, v26, v23
	s_waitcnt lgkmcnt(7)
	v_mul_f32_e32 v23, v4, v83
	v_fmac_f32_e32 v23, v2, v82
	v_fmac_f32_e32 v23, v5, v84
	v_fmac_f32_e32 v23, v3, v85
	ds_read_b128 v[82:85], v188 offset:432
	v_add_f32_e32 v22, v26, v23
	v_min_f32_e32 v23, 0, v22
	v_mul_f32_e64 v22, |v22|, s24
	v_exp_f32_e32 v22, v22
	s_nop 0
	v_add_f32_e32 v22, 1.0, v22
	v_log_f32_e32 v22, v22
	s_nop 0
	v_fmac_f32_e32 v23, 0xbf317218, v22
	v_fmamk_f32 v22, v23, 0x3d800000, v21
	s_waitcnt lgkmcnt(7)
	v_mul_f32_e32 v23, v15, v87
	v_fmac_f32_e32 v23, v14, v86
	v_fmac_f32_e32 v23, v16, v88
	v_fmac_f32_e32 v23, v17, v89
	ds_read_b128 v[86:89], v188 offset:448
	v_add_f32_e32 v23, v18, v23
	s_waitcnt lgkmcnt(7)
	v_mul_f32_e32 v25, v7, v93
	v_fmac_f32_e32 v25, v6, v92
	v_fmac_f32_e32 v25, v10, v94
	v_fmac_f32_e32 v25, v11, v95
	ds_read_b128 v[92:95], v188 offset:464
	v_add_f32_e32 v23, v23, v25
	s_waitcnt lgkmcnt(7)
	v_mul_f32_e32 v25, v9, v97
	v_fmac_f32_e32 v25, v8, v96
	v_fmac_f32_e32 v25, v12, v98
	v_fmac_f32_e32 v25, v13, v99
	ds_read_b128 v[96:99], v188 offset:480
	v_add_f32_e32 v23, v23, v25
	s_waitcnt lgkmcnt(7)
	v_mul_f32_e32 v25, v4, v101
	v_fmac_f32_e32 v25, v2, v100
	v_fmac_f32_e32 v25, v5, v102
	v_fmac_f32_e32 v25, v3, v103
	ds_read_b128 v[100:103], v188 offset:496
	v_add_f32_e32 v23, v23, v25
	v_min_f32_e32 v24, 0, v23
	v_mul_f32_e64 v23, |v23|, s24
	v_exp_f32_e32 v23, v23
	s_nop 0
	v_add_f32_e32 v23, 1.0, v23
	v_log_f32_e32 v23, v23
	s_nop 0
	v_fmac_f32_e32 v24, 0xbf317218, v23
	v_fmamk_f32 v23, v24, 0x3d800000, v22
	s_waitcnt lgkmcnt(7)
	v_mul_f32_e32 v25, v15, v39
	v_fmac_f32_e32 v25, v14, v38
	v_fmac_f32_e32 v25, v16, v40
	v_fmac_f32_e32 v25, v17, v41
	ds_read_b128 v[38:41], v188 offset:512
	v_add_f32_e32 v28, v18, v25
	s_waitcnt lgkmcnt(7)
	v_mul_f32_e32 v25, v7, v43
	v_fmac_f32_e32 v25, v6, v42
	v_fmac_f32_e32 v25, v10, v44
	v_fmac_f32_e32 v25, v11, v45
	ds_read_b128 v[42:45], v188 offset:528
	v_add_f32_e32 v28, v28, v25
	s_waitcnt lgkmcnt(7)
	v_mul_f32_e32 v25, v9, v47
	v_fmac_f32_e32 v25, v8, v46
	v_fmac_f32_e32 v25, v12, v48
	v_fmac_f32_e32 v25, v13, v49
	ds_read_b128 v[46:49], v188 offset:544
	v_add_f32_e32 v28, v28, v25
	s_waitcnt lgkmcnt(7)
	v_mul_f32_e32 v25, v4, v83
	v_fmac_f32_e32 v25, v2, v82
	v_fmac_f32_e32 v25, v5, v84
	v_fmac_f32_e32 v25, v3, v85
	ds_read_b128 v[82:85], v188 offset:560
	v_add_f32_e32 v24, v28, v25
	v_min_f32_e32 v25, 0, v24
	v_mul_f32_e64 v24, |v24|, s24
	v_exp_f32_e32 v24, v24
	s_nop 0
	v_add_f32_e32 v24, 1.0, v24
	v_log_f32_e32 v24, v24
	s_nop 0
	v_fmac_f32_e32 v25, 0xbf317218, v24
	v_fmamk_f32 v24, v25, 0x3d800000, v23
	s_waitcnt lgkmcnt(7)
	v_mul_f32_e32 v25, v15, v87
	v_fmac_f32_e32 v25, v14, v86
	v_fmac_f32_e32 v25, v16, v88
	v_fmac_f32_e32 v25, v17, v89
	ds_read_b128 v[86:89], v188 offset:576
	v_add_f32_e32 v25, v18, v25
	s_waitcnt lgkmcnt(7)
	v_mul_f32_e32 v27, v7, v93
	v_fmac_f32_e32 v27, v6, v92
	v_fmac_f32_e32 v27, v10, v94
	v_fmac_f32_e32 v27, v11, v95
	ds_read_b128 v[92:95], v188 offset:592
	v_add_f32_e32 v25, v25, v27
	s_waitcnt lgkmcnt(7)
	v_mul_f32_e32 v27, v9, v97
	v_fmac_f32_e32 v27, v8, v96
	v_fmac_f32_e32 v27, v12, v98
	v_fmac_f32_e32 v27, v13, v99
	ds_read_b128 v[96:99], v188 offset:608
	v_add_f32_e32 v25, v25, v27
	s_waitcnt lgkmcnt(7)
	v_mul_f32_e32 v27, v4, v101
	v_fmac_f32_e32 v27, v2, v100
	v_fmac_f32_e32 v27, v5, v102
	v_fmac_f32_e32 v27, v3, v103
	ds_read_b128 v[100:103], v188 offset:624
	v_add_f32_e32 v25, v25, v27
	v_min_f32_e32 v26, 0, v25
	v_mul_f32_e64 v25, |v25|, s24
	v_exp_f32_e32 v25, v25
	s_nop 0
	v_add_f32_e32 v25, 1.0, v25
	v_log_f32_e32 v25, v25
	s_nop 0
	v_fmac_f32_e32 v26, 0xbf317218, v25
	v_fmamk_f32 v25, v26, 0x3d800000, v24
	s_waitcnt lgkmcnt(7)
	v_mul_f32_e32 v27, v15, v39
	v_fmac_f32_e32 v27, v14, v38
	v_fmac_f32_e32 v27, v16, v40
	v_fmac_f32_e32 v27, v17, v41
	ds_read_b128 v[38:41], v188 offset:640
	v_add_f32_e32 v30, v18, v27
	s_waitcnt lgkmcnt(7)
	v_mul_f32_e32 v27, v7, v43
	v_fmac_f32_e32 v27, v6, v42
	v_fmac_f32_e32 v27, v10, v44
	v_fmac_f32_e32 v27, v11, v45
	ds_read_b128 v[42:45], v188 offset:656
	v_add_f32_e32 v30, v30, v27
	s_waitcnt lgkmcnt(7)
	v_mul_f32_e32 v27, v9, v47
	v_fmac_f32_e32 v27, v8, v46
	v_fmac_f32_e32 v27, v12, v48
	v_fmac_f32_e32 v27, v13, v49
	ds_read_b128 v[46:49], v188 offset:672
	v_add_f32_e32 v30, v30, v27
	s_waitcnt lgkmcnt(7)
	v_mul_f32_e32 v27, v4, v83
	v_fmac_f32_e32 v27, v2, v82
	v_fmac_f32_e32 v27, v5, v84
	v_fmac_f32_e32 v27, v3, v85
	ds_read_b128 v[82:85], v188 offset:688
	v_add_f32_e32 v26, v30, v27
	v_min_f32_e32 v27, 0, v26
	v_mul_f32_e64 v26, |v26|, s24
	v_exp_f32_e32 v26, v26
	s_nop 0
	v_add_f32_e32 v26, 1.0, v26
	v_log_f32_e32 v26, v26
	s_nop 0
	v_fmac_f32_e32 v27, 0xbf317218, v26
	v_fmamk_f32 v26, v27, 0x3d800000, v25
	s_waitcnt lgkmcnt(7)
	v_mul_f32_e32 v27, v15, v87
	v_fmac_f32_e32 v27, v14, v86
	v_fmac_f32_e32 v27, v16, v88
	v_fmac_f32_e32 v27, v17, v89
	ds_read_b128 v[86:89], v188 offset:704
	v_add_f32_e32 v27, v18, v27
	s_waitcnt lgkmcnt(7)
	v_mul_f32_e32 v29, v7, v93
	v_fmac_f32_e32 v29, v6, v92
	v_fmac_f32_e32 v29, v10, v94
	v_fmac_f32_e32 v29, v11, v95
	ds_read_b128 v[92:95], v188 offset:720
	v_add_f32_e32 v27, v27, v29
	s_waitcnt lgkmcnt(7)
	v_mul_f32_e32 v29, v9, v97
	v_fmac_f32_e32 v29, v8, v96
	v_fmac_f32_e32 v29, v12, v98
	v_fmac_f32_e32 v29, v13, v99
	ds_read_b128 v[96:99], v188 offset:736
	v_add_f32_e32 v27, v27, v29
	s_waitcnt lgkmcnt(7)
	v_mul_f32_e32 v29, v4, v101
	v_fmac_f32_e32 v29, v2, v100
	v_fmac_f32_e32 v29, v5, v102
	v_fmac_f32_e32 v29, v3, v103
	ds_read_b128 v[100:103], v188 offset:752
	v_add_f32_e32 v27, v27, v29
	v_min_f32_e32 v28, 0, v27
	v_mul_f32_e64 v27, |v27|, s24
	v_exp_f32_e32 v27, v27
	s_nop 0
	v_add_f32_e32 v27, 1.0, v27
	v_log_f32_e32 v27, v27
	s_nop 0
	v_fmac_f32_e32 v28, 0xbf317218, v27
	v_fmamk_f32 v27, v28, 0x3d800000, v26
	s_waitcnt lgkmcnt(7)
	v_mul_f32_e32 v29, v15, v39
	v_fmac_f32_e32 v29, v14, v38
	v_fmac_f32_e32 v29, v16, v40
	v_fmac_f32_e32 v29, v17, v41
	ds_read_b128 v[38:41], v188 offset:768
	v_add_f32_e32 v32, v18, v29
	s_waitcnt lgkmcnt(7)
	v_mul_f32_e32 v29, v7, v43
	v_fmac_f32_e32 v29, v6, v42
	v_fmac_f32_e32 v29, v10, v44
	v_fmac_f32_e32 v29, v11, v45
	ds_read_b128 v[42:45], v188 offset:784
	v_add_f32_e32 v32, v32, v29
	s_waitcnt lgkmcnt(7)
	v_mul_f32_e32 v29, v9, v47
	v_fmac_f32_e32 v29, v8, v46
	v_fmac_f32_e32 v29, v12, v48
	v_fmac_f32_e32 v29, v13, v49
	ds_read_b128 v[46:49], v188 offset:800
	v_add_f32_e32 v32, v32, v29
	s_waitcnt lgkmcnt(7)
	v_mul_f32_e32 v29, v4, v83
	v_fmac_f32_e32 v29, v2, v82
	v_fmac_f32_e32 v29, v5, v84
	v_fmac_f32_e32 v29, v3, v85
	ds_read_b128 v[82:85], v188 offset:816
	v_add_f32_e32 v28, v32, v29
	v_min_f32_e32 v29, 0, v28
	v_mul_f32_e64 v28, |v28|, s24
	v_exp_f32_e32 v28, v28
	s_nop 0
	v_add_f32_e32 v28, 1.0, v28
	v_log_f32_e32 v28, v28
	s_nop 0
	v_fmac_f32_e32 v29, 0xbf317218, v28
	v_fmamk_f32 v28, v29, 0x3d800000, v27
	s_waitcnt lgkmcnt(7)
	v_mul_f32_e32 v29, v15, v87
	v_fmac_f32_e32 v29, v14, v86
	v_fmac_f32_e32 v29, v16, v88
	v_fmac_f32_e32 v29, v17, v89
	ds_read_b128 v[86:89], v188 offset:832
	v_add_f32_e32 v29, v18, v29
	s_waitcnt lgkmcnt(7)
	v_mul_f32_e32 v31, v7, v93
	v_fmac_f32_e32 v31, v6, v92
	v_fmac_f32_e32 v31, v10, v94
	v_fmac_f32_e32 v31, v11, v95
	ds_read_b128 v[92:95], v188 offset:848
	v_add_f32_e32 v29, v29, v31
	s_waitcnt lgkmcnt(7)
	v_mul_f32_e32 v31, v9, v97
	v_fmac_f32_e32 v31, v8, v96
	v_fmac_f32_e32 v31, v12, v98
	v_fmac_f32_e32 v31, v13, v99
	ds_read_b128 v[96:99], v188 offset:864
	v_add_f32_e32 v29, v29, v31
	s_waitcnt lgkmcnt(7)
	v_mul_f32_e32 v31, v4, v101
	v_fmac_f32_e32 v31, v2, v100
	v_fmac_f32_e32 v31, v5, v102
	v_fmac_f32_e32 v31, v3, v103
	ds_read_b128 v[100:103], v188 offset:880
	v_add_f32_e32 v29, v29, v31
	v_min_f32_e32 v30, 0, v29
	v_mul_f32_e64 v29, |v29|, s24
	v_exp_f32_e32 v29, v29
	s_nop 0
	v_add_f32_e32 v29, 1.0, v29
	v_log_f32_e32 v29, v29
	s_nop 0
	v_fmac_f32_e32 v30, 0xbf317218, v29
	v_fmamk_f32 v29, v30, 0x3d800000, v28
	s_waitcnt lgkmcnt(7)
	v_mul_f32_e32 v31, v15, v39
	v_fmac_f32_e32 v31, v14, v38
	v_fmac_f32_e32 v31, v16, v40
	v_fmac_f32_e32 v31, v17, v41
	ds_read_b128 v[38:41], v188 offset:896
	v_add_f32_e32 v34, v18, v31
	s_waitcnt lgkmcnt(7)
	v_mul_f32_e32 v31, v7, v43
	v_fmac_f32_e32 v31, v6, v42
	v_fmac_f32_e32 v31, v10, v44
	v_fmac_f32_e32 v31, v11, v45
	ds_read_b128 v[42:45], v188 offset:912
	v_add_f32_e32 v34, v34, v31
	s_waitcnt lgkmcnt(7)
	v_mul_f32_e32 v31, v9, v47
	v_fmac_f32_e32 v31, v8, v46
	v_fmac_f32_e32 v31, v12, v48
	v_fmac_f32_e32 v31, v13, v49
	ds_read_b128 v[46:49], v188 offset:928
	v_add_f32_e32 v34, v34, v31
	s_waitcnt lgkmcnt(7)
	v_mul_f32_e32 v31, v4, v83
	v_fmac_f32_e32 v31, v2, v82
	v_fmac_f32_e32 v31, v5, v84
	v_fmac_f32_e32 v31, v3, v85
	ds_read_b128 v[82:85], v188 offset:944
	v_add_f32_e32 v30, v34, v31
	v_min_f32_e32 v31, 0, v30
	v_mul_f32_e64 v30, |v30|, s24
	v_exp_f32_e32 v30, v30
	s_nop 0
	v_add_f32_e32 v30, 1.0, v30
	v_log_f32_e32 v30, v30
	s_nop 0
	v_fmac_f32_e32 v31, 0xbf317218, v30
	v_fmamk_f32 v30, v31, 0x3d800000, v29
	s_waitcnt lgkmcnt(7)
	v_mul_f32_e32 v31, v15, v87
	v_fmac_f32_e32 v31, v14, v86
	v_fmac_f32_e32 v31, v16, v88
	v_fmac_f32_e32 v31, v17, v89
	ds_read_b128 v[86:89], v188 offset:960
	v_add_f32_e32 v31, v18, v31
	s_waitcnt lgkmcnt(7)
	v_mul_f32_e32 v33, v7, v93
	v_fmac_f32_e32 v33, v6, v92
	v_fmac_f32_e32 v33, v10, v94
	v_fmac_f32_e32 v33, v11, v95
	ds_read_b128 v[92:95], v188 offset:976
	v_add_f32_e32 v31, v31, v33
	s_waitcnt lgkmcnt(7)
	v_mul_f32_e32 v33, v9, v97
	v_fmac_f32_e32 v33, v8, v96
	v_fmac_f32_e32 v33, v12, v98
	v_fmac_f32_e32 v33, v13, v99
	ds_read_b128 v[96:99], v188 offset:992
	v_add_f32_e32 v31, v31, v33
	s_waitcnt lgkmcnt(7)
	v_mul_f32_e32 v33, v4, v101
	v_fmac_f32_e32 v33, v2, v100
	v_fmac_f32_e32 v33, v5, v102
	v_fmac_f32_e32 v33, v3, v103
	ds_read_b128 v[100:103], v188 offset:1008
	v_add_f32_e32 v31, v31, v33
	v_min_f32_e32 v32, 0, v31
	v_mul_f32_e64 v31, |v31|, s24
	v_exp_f32_e32 v31, v31
	s_nop 0
	v_add_f32_e32 v31, 1.0, v31
	v_log_f32_e32 v31, v31
	s_nop 0
	v_fmac_f32_e32 v32, 0xbf317218, v31
	v_fmamk_f32 v31, v32, 0x3d800000, v30
	s_waitcnt lgkmcnt(7)
	v_mul_f32_e32 v33, v15, v39
	v_fmac_f32_e32 v33, v14, v38
	v_fmac_f32_e32 v33, v16, v40
	v_fmac_f32_e32 v33, v17, v41
	v_add_f32_e32 v36, v18, v33
	s_waitcnt lgkmcnt(6)
	v_mul_f32_e32 v33, v7, v43
	v_fmac_f32_e32 v33, v6, v42
	v_fmac_f32_e32 v33, v10, v44
	v_fmac_f32_e32 v33, v11, v45
	v_add_f32_e32 v36, v36, v33
	s_waitcnt lgkmcnt(5)
	v_mul_f32_e32 v33, v9, v47
	v_fmac_f32_e32 v33, v8, v46
	v_fmac_f32_e32 v33, v12, v48
	v_fmac_f32_e32 v33, v13, v49
	v_add_f32_e32 v36, v36, v33
	s_waitcnt lgkmcnt(4)
	v_mul_f32_e32 v33, v4, v83
	v_fmac_f32_e32 v33, v2, v82
	v_fmac_f32_e32 v33, v5, v84
	v_fmac_f32_e32 v33, v3, v85
	v_add_f32_e32 v32, v36, v33
	v_min_f32_e32 v33, 0, v32
	v_mul_f32_e64 v32, |v32|, s24
	v_exp_f32_e32 v32, v32
	s_nop 0
	v_add_f32_e32 v32, 1.0, v32
	v_log_f32_e32 v32, v32
	s_nop 0
	v_fmac_f32_e32 v33, 0xbf317218, v32
	v_fmamk_f32 v36, v33, 0x3d800000, v31
	s_waitcnt lgkmcnt(3)
	v_mul_f32_e32 v15, v15, v87
	v_fmac_f32_e32 v15, v14, v86
	v_fmac_f32_e32 v15, v16, v88
	v_fmac_f32_e32 v15, v17, v89
	v_add_f32_e32 v18, v18, v15
	s_waitcnt lgkmcnt(2)
	v_mul_f32_e32 v7, v7, v93
	v_fmac_f32_e32 v7, v6, v92
	v_fmac_f32_e32 v7, v10, v94
	v_fmac_f32_e32 v7, v11, v95
	v_add_f32_e32 v6, v18, v7
	s_waitcnt lgkmcnt(1)
	v_mul_f32_e32 v7, v9, v97
	v_fmac_f32_e32 v7, v8, v96
	v_fmac_f32_e32 v7, v12, v98
	v_fmac_f32_e32 v7, v13, v99
	v_add_f32_e32 v10, v6, v7
	s_waitcnt lgkmcnt(0)
	v_mul_f32_e32 v4, v4, v101
	v_fmac_f32_e32 v4, v2, v100
	v_fmac_f32_e32 v4, v5, v102
	v_fmac_f32_e32 v4, v3, v103
	v_add_f32_e32 v2, v10, v4
	v_min_f32_e32 v3, 0, v2
	v_mul_f32_e64 v2, |v2|, s24
	v_exp_f32_e32 v2, v2
	s_nop 0
	v_add_f32_e32 v2, 1.0, v2
	v_log_f32_e32 v2, v2
	s_nop 0
	v_fmac_f32_e32 v3, 0xbf317218, v2
	v_fmamk_f32 v4, v3, 0x3d800000, v36
	ds_write_b32 v187, v4 offset:4096
	s_waitcnt lgkmcnt(0)
	s_barrier
	ds_read2st64_b32 v[2:3], v189 offset0:16 offset1:18
	s_waitcnt lgkmcnt(0)
	v_add_f32_e32 v2, 0, v2
	v_cndmask_b32_e64 v2, 0, v2, s[38:39]
	v_cndmask_b32_e64 v3, 0, v3, s[40:41]
	v_add_f32_e32 v5, v2, v3
	ds_read2st64_b32 v[2:3], v189 offset0:20 offset1:22
	s_waitcnt lgkmcnt(0)
	v_cndmask_b32_e64 v2, 0, v2, s[42:43]
	v_add_f32_e32 v2, v5, v2
	v_cndmask_b32_e64 v3, 0, v3, s[44:45]
	v_add_f32_e32 v3, v2, v3
	v_add_f32_e32 v11, v0, v3
	v_add_f32_e32 v13, v20, v3
	v_add_f32_e32 v0, v3, v4
	v_lshlrev_b32_e32 v4, 1, v161
	v_lshlrev_b32_e32 v20, 5, v161
	v_add_f32_e32 v12, v19, v3
	v_add_f32_e32 v14, v21, v3
	v_add_f32_e32 v15, v22, v3
	v_add_f32_e32 v16, v23, v3
	v_add_f32_e32 v17, v24, v3
	v_add_f32_e32 v18, v25, v3
	v_add_f32_e32 v10, v26, v3
	v_add_f32_e32 v9, v27, v3
	v_add_f32_e32 v8, v28, v3
	v_add_f32_e32 v7, v29, v3
	v_add_f32_e32 v6, v30, v3
	v_add_f32_e32 v5, v31, v3
	v_add_f32_e32 v2, v3, v36
	v_and_b32_e32 v3, 14, v4
	v_and_b32_e32 v20, 0xfffff000, v20
	v_add_u32_e32 v3, 0, v3
	v_and_or_b32 v4, v4, s20, v20
	v_add_u32_e32 v20, v3, v4
	ds_read_u16 v21, v20 offset:8192
	v_mul_f32_e32 v11, 0x3fb8aa3b, v11
	v_exp_f32_e32 v11, v11
	v_mul_f32_e32 v10, 0x3fb8aa3b, v10
	v_exp_f32_e32 v10, v10
	s_waitcnt lgkmcnt(0)
	v_lshlrev_b32_e32 v21, 16, v21
	v_mul_f32_e32 v21, 0x3db504f3, v21
	v_rcp_f32_e32 v19, v11
	v_mul_f32_e32 v11, v11, v21
	ds_read_u16 v21, v20 offset:24576
	v_mul_f32_e32 v9, 0x3fb8aa3b, v9
	v_exp_f32_e32 v9, v9
	v_mul_f32_e32 v8, 0x3fb8aa3b, v8
	v_exp_f32_e32 v8, v8
	s_waitcnt lgkmcnt(0)
	v_lshlrev_b32_e32 v21, 16, v21
	v_mul_f32_e32 v19, v19, v21
	v_bfe_u32 v21, v11, 16, 1
	v_add3_u32 v11, v11, v21, s18
	ds_write_b16_d16_hi v20, v11 offset:8192
	v_bfe_u32 v11, v19, 16, 1
	v_add3_u32 v11, v19, v11, s18
	ds_write_b16_d16_hi v20, v11 offset:24576
	v_xad_u32 v19, v4, 64, v3
	ds_read_u16 v20, v19 offset:8448
	v_mul_f32_e32 v11, 0x3fb8aa3b, v12
	v_exp_f32_e32 v11, v11
	v_mul_f32_e32 v7, 0x3fb8aa3b, v7
	v_exp_f32_e32 v7, v7
	s_waitcnt lgkmcnt(0)
	v_lshlrev_b32_e32 v20, 16, v20
	v_mul_f32_e32 v20, 0x3db504f3, v20
	v_rcp_f32_e32 v12, v11
	v_mul_f32_e32 v11, v11, v20
	ds_read_u16 v20, v19 offset:24832
	v_mul_f32_e32 v6, 0x3fb8aa3b, v6
	v_exp_f32_e32 v6, v6
	v_mul_f32_e32 v5, 0x3fb8aa3b, v5
	v_exp_f32_e32 v5, v5
	s_waitcnt lgkmcnt(0)
	v_lshlrev_b32_e32 v20, 16, v20
	v_mul_f32_e32 v12, v12, v20
	v_bfe_u32 v20, v11, 16, 1
	v_add3_u32 v11, v11, v20, s18
	ds_write_b16_d16_hi v19, v11 offset:8448
	v_bfe_u32 v11, v12, 16, 1
	v_add3_u32 v11, v12, v11, s18
	ds_write_b16_d16_hi v19, v11 offset:24832
	v_mul_f32_e32 v11, 0x3fb8aa3b, v13
	v_xad_u32 v13, v4, s12, v3
	ds_read_u16 v19, v13 offset:8704
	v_exp_f32_e32 v11, v11
	s_movk_i32 s12, 0xc0
	v_mul_f32_e32 v2, 0x3fb8aa3b, v2
	v_exp_f32_e32 v2, v2
	s_waitcnt lgkmcnt(0)
	v_lshlrev_b32_e32 v19, 16, v19
	v_mul_f32_e32 v19, 0x3db504f3, v19
	v_rcp_f32_e32 v12, v11
	v_mul_f32_e32 v11, v11, v19
	ds_read_u16 v19, v13 offset:25088
	v_mul_f32_e32 v0, 0x3fb8aa3b, v0
	v_exp_f32_e32 v0, v0
	s_waitcnt lgkmcnt(0)
	v_lshlrev_b32_e32 v19, 16, v19
	v_mul_f32_e32 v12, v12, v19
	v_bfe_u32 v19, v11, 16, 1
	v_add3_u32 v11, v11, v19, s18
	ds_write_b16_d16_hi v13, v11 offset:8704
	v_bfe_u32 v11, v12, 16, 1
	v_add3_u32 v11, v12, v11, s18
	ds_write_b16_d16_hi v13, v11 offset:25088
	v_xad_u32 v13, v4, s12, v3
	v_mul_f32_e32 v11, 0x3fb8aa3b, v14
	ds_read_u16 v14, v13 offset:8960
	v_exp_f32_e32 v11, v11
	s_movk_i32 s12, 0x50
	s_waitcnt lgkmcnt(0)
	v_lshlrev_b32_e32 v14, 16, v14
	v_mul_f32_e32 v14, 0x3db504f3, v14
	v_rcp_f32_e32 v12, v11
	v_mul_f32_e32 v11, v11, v14
	ds_read_u16 v14, v13 offset:25344
	s_waitcnt lgkmcnt(0)
	v_lshlrev_b32_e32 v14, 16, v14
	v_mul_f32_e32 v12, v12, v14
	v_bfe_u32 v14, v11, 16, 1
	v_add3_u32 v11, v11, v14, s18
	ds_write_b16_d16_hi v13, v11 offset:8960
	v_bfe_u32 v11, v12, 16, 1
	v_add3_u32 v11, v12, v11, s18
	ds_write_b16_d16_hi v13, v11 offset:25344
	v_xad_u32 v13, v4, 16, v3
	ds_read_u16 v14, v13 offset:9216
	v_mul_f32_e32 v11, 0x3fb8aa3b, v15
	v_exp_f32_e32 v11, v11
	s_waitcnt lgkmcnt(0)
	v_lshlrev_b32_e32 v14, 16, v14
	v_mul_f32_e32 v14, 0x3db504f3, v14
	v_rcp_f32_e32 v12, v11
	v_mul_f32_e32 v11, v11, v14
	ds_read_u16 v14, v13 offset:25600
	s_waitcnt lgkmcnt(0)
	v_lshlrev_b32_e32 v14, 16, v14
	v_mul_f32_e32 v12, v12, v14
	v_bfe_u32 v14, v11, 16, 1
	v_add3_u32 v11, v11, v14, s18
	ds_write_b16_d16_hi v13, v11 offset:9216
	v_bfe_u32 v11, v12, 16, 1
	v_add3_u32 v11, v12, v11, s18
	ds_write_b16_d16_hi v13, v11 offset:25600
	v_xad_u32 v13, v4, s12, v3
	ds_read_u16 v14, v13 offset:9472
	v_mul_f32_e32 v11, 0x3fb8aa3b, v16
	v_exp_f32_e32 v11, v11
	s_movk_i32 s12, 0x90
	s_waitcnt lgkmcnt(0)
	v_lshlrev_b32_e32 v14, 16, v14
	v_mul_f32_e32 v14, 0x3db504f3, v14
	v_rcp_f32_e32 v12, v11
	v_mul_f32_e32 v11, v11, v14
	ds_read_u16 v14, v13 offset:25856
	s_waitcnt lgkmcnt(0)
	v_lshlrev_b32_e32 v14, 16, v14
	v_mul_f32_e32 v12, v12, v14
	v_bfe_u32 v14, v11, 16, 1
	v_add3_u32 v11, v11, v14, s18
	ds_write_b16_d16_hi v13, v11 offset:9472
	v_bfe_u32 v11, v12, 16, 1
	v_add3_u32 v11, v12, v11, s18
	ds_write_b16_d16_hi v13, v11 offset:25856
	v_xad_u32 v13, v4, s12, v3
	ds_read_u16 v14, v13 offset:9728
	v_mul_f32_e32 v11, 0x3fb8aa3b, v17
	v_exp_f32_e32 v11, v11
	s_movk_i32 s12, 0xd0
	s_waitcnt lgkmcnt(0)
	v_lshlrev_b32_e32 v14, 16, v14
	v_mul_f32_e32 v14, 0x3db504f3, v14
	v_rcp_f32_e32 v12, v11
	v_mul_f32_e32 v11, v11, v14
	ds_read_u16 v14, v13 offset:26112
	s_waitcnt lgkmcnt(0)
	v_lshlrev_b32_e32 v14, 16, v14
	v_mul_f32_e32 v12, v12, v14
	v_bfe_u32 v14, v11, 16, 1
	v_add3_u32 v11, v11, v14, s18
	ds_write_b16_d16_hi v13, v11 offset:9728
	v_bfe_u32 v11, v12, 16, 1
	v_add3_u32 v11, v12, v11, s18
	ds_write_b16_d16_hi v13, v11 offset:26112
	v_xad_u32 v13, v4, s12, v3
	ds_read_u16 v14, v13 offset:9984
	v_mul_f32_e32 v11, 0x3fb8aa3b, v18
	v_exp_f32_e32 v11, v11
	s_movk_i32 s12, 0x60
	s_waitcnt lgkmcnt(0)
	v_lshlrev_b32_e32 v14, 16, v14
	v_mul_f32_e32 v14, 0x3db504f3, v14
	v_rcp_f32_e32 v12, v11
	v_mul_f32_e32 v11, v11, v14
	ds_read_u16 v14, v13 offset:26368
	s_waitcnt lgkmcnt(0)
	v_lshlrev_b32_e32 v14, 16, v14
	v_mul_f32_e32 v12, v12, v14
	v_bfe_u32 v14, v11, 16, 1
	v_add3_u32 v11, v11, v14, s18
	ds_write_b16_d16_hi v13, v11 offset:9984
	v_bfe_u32 v11, v12, 16, 1
	v_add3_u32 v11, v12, v11, s18
	ds_write_b16_d16_hi v13, v11 offset:26368
	v_xad_u32 v12, v4, 32, v3
	ds_read_u16 v13, v12 offset:10240
	v_rcp_f32_e32 v11, v10
	s_waitcnt lgkmcnt(0)
	v_lshlrev_b32_e32 v13, 16, v13
	v_mul_f32_e32 v13, 0x3db504f3, v13
	v_mul_f32_e32 v10, v10, v13
	ds_read_u16 v13, v12 offset:26624
	s_waitcnt lgkmcnt(0)
	v_lshlrev_b32_e32 v13, 16, v13
	v_mul_f32_e32 v11, v11, v13
	v_bfe_u32 v13, v10, 16, 1
	v_add3_u32 v10, v10, v13, s18
	ds_write_b16_d16_hi v12, v10 offset:10240
	v_bfe_u32 v10, v11, 16, 1
	v_add3_u32 v10, v11, v10, s18
	ds_write_b16_d16_hi v12, v10 offset:26624
	v_xad_u32 v11, v4, s12, v3
	ds_read_u16 v12, v11 offset:10496
	v_rcp_f32_e32 v10, v9
	s_movk_i32 s12, 0xa0
	s_waitcnt lgkmcnt(0)
	v_lshlrev_b32_e32 v12, 16, v12
	v_mul_f32_e32 v12, 0x3db504f3, v12
	v_mul_f32_e32 v9, v9, v12
	ds_read_u16 v12, v11 offset:26880
	s_waitcnt lgkmcnt(0)
	v_lshlrev_b32_e32 v12, 16, v12
	v_mul_f32_e32 v10, v10, v12
	v_bfe_u32 v12, v9, 16, 1
	v_add3_u32 v9, v9, v12, s18
	ds_write_b16_d16_hi v11, v9 offset:10496
	v_bfe_u32 v9, v10, 16, 1
	v_add3_u32 v9, v10, v9, s18
	ds_write_b16_d16_hi v11, v9 offset:26880
	v_xad_u32 v10, v4, s12, v3
	ds_read_u16 v11, v10 offset:10752
	v_rcp_f32_e32 v9, v8
	s_movk_i32 s12, 0xe0
	s_waitcnt lgkmcnt(0)
	v_lshlrev_b32_e32 v11, 16, v11
	v_mul_f32_e32 v11, 0x3db504f3, v11
	v_mul_f32_e32 v8, v8, v11
	ds_read_u16 v11, v10 offset:27136
	s_waitcnt lgkmcnt(0)
	v_lshlrev_b32_e32 v11, 16, v11
	v_mul_f32_e32 v9, v9, v11
	v_bfe_u32 v11, v8, 16, 1
	v_add3_u32 v8, v8, v11, s18
	ds_write_b16_d16_hi v10, v8 offset:10752
	v_bfe_u32 v8, v9, 16, 1
	v_add3_u32 v8, v9, v8, s18
	ds_write_b16_d16_hi v10, v8 offset:27136
	v_xad_u32 v9, v4, s12, v3
	ds_read_u16 v10, v9 offset:11008
	v_rcp_f32_e32 v8, v7
	s_movk_i32 s12, 0x70
	s_waitcnt lgkmcnt(0)
	v_lshlrev_b32_e32 v10, 16, v10
	v_mul_f32_e32 v10, 0x3db504f3, v10
	v_mul_f32_e32 v7, v7, v10
	ds_read_u16 v10, v9 offset:27392
	s_waitcnt lgkmcnt(0)
	v_lshlrev_b32_e32 v10, 16, v10
	v_mul_f32_e32 v8, v8, v10
	v_bfe_u32 v10, v7, 16, 1
	v_add3_u32 v7, v7, v10, s18
	ds_write_b16_d16_hi v9, v7 offset:11008
	v_bfe_u32 v7, v8, 16, 1
	v_add3_u32 v7, v8, v7, s18
	ds_write_b16_d16_hi v9, v7 offset:27392
	v_xad_u32 v8, v4, 48, v3
	ds_read_u16 v9, v8 offset:11264
	v_rcp_f32_e32 v7, v6
	s_waitcnt lgkmcnt(0)
	v_lshlrev_b32_e32 v9, 16, v9
	v_mul_f32_e32 v9, 0x3db504f3, v9
	v_mul_f32_e32 v6, v6, v9
	ds_read_u16 v9, v8 offset:27648
	s_waitcnt lgkmcnt(0)
	v_lshlrev_b32_e32 v9, 16, v9
	v_mul_f32_e32 v7, v7, v9
	v_bfe_u32 v9, v6, 16, 1
	v_add3_u32 v6, v6, v9, s18
	ds_write_b16_d16_hi v8, v6 offset:11264
	v_bfe_u32 v6, v7, 16, 1
	v_add3_u32 v6, v7, v6, s18
	ds_write_b16_d16_hi v8, v6 offset:27648
	v_xad_u32 v7, v4, s12, v3
	ds_read_u16 v8, v7 offset:11520
	v_rcp_f32_e32 v6, v5
	s_movk_i32 s12, 0xb0
	s_waitcnt lgkmcnt(0)
	v_lshlrev_b32_e32 v8, 16, v8
	v_mul_f32_e32 v8, 0x3db504f3, v8
	v_mul_f32_e32 v5, v5, v8
	ds_read_u16 v8, v7 offset:27904
	s_waitcnt lgkmcnt(0)
	v_lshlrev_b32_e32 v8, 16, v8
	v_mul_f32_e32 v6, v6, v8
	v_bfe_u32 v8, v5, 16, 1
	v_add3_u32 v5, v5, v8, s18
	ds_write_b16_d16_hi v7, v5 offset:11520
	v_bfe_u32 v5, v6, 16, 1
	v_add3_u32 v5, v6, v5, s18
	ds_write_b16_d16_hi v7, v5 offset:27904
	v_xad_u32 v6, v4, s12, v3
	ds_read_u16 v7, v6 offset:11776
	v_rcp_f32_e32 v5, v2
	v_xad_u32 v3, v4, s20, v3
	v_readlane_b32 s12, v253, 32
	s_waitcnt lgkmcnt(0)
	v_lshlrev_b32_e32 v7, 16, v7
	v_mul_f32_e32 v7, 0x3db504f3, v7
	v_mul_f32_e32 v2, v2, v7
	ds_read_u16 v7, v6 offset:28160
	s_waitcnt lgkmcnt(0)
	v_lshlrev_b32_e32 v7, 16, v7
	v_mul_f32_e32 v5, v5, v7
	v_bfe_u32 v7, v2, 16, 1
	v_add3_u32 v2, v2, v7, s18
	ds_write_b16_d16_hi v6, v2 offset:11776
	v_bfe_u32 v2, v5, 16, 1
	v_add3_u32 v2, v5, v2, s18
	ds_write_b16_d16_hi v6, v2 offset:28160
	ds_read_u16 v4, v3 offset:12032
	v_rcp_f32_e32 v2, v0
	s_waitcnt lgkmcnt(0)
	v_lshlrev_b32_e32 v4, 16, v4
	v_mul_f32_e32 v4, 0x3db504f3, v4
	v_mul_f32_e32 v0, v0, v4
	ds_read_u16 v4, v3 offset:28416
	s_waitcnt lgkmcnt(0)
	v_lshlrev_b32_e32 v4, 16, v4
	v_mul_f32_e32 v2, v2, v4
	v_bfe_u32 v4, v0, 16, 1
	v_add3_u32 v0, v0, v4, s18
	ds_write_b16_d16_hi v3, v0 offset:12032
	v_bfe_u32 v0, v2, 16, 1
	v_add3_u32 v0, v2, v0, s18
	ds_write_b16_d16_hi v3, v0 offset:28416
	v_lshlrev_b32_e32 v0, 2, v197
	v_and_b32_e32 v200, 12, v0
	v_bitop3_b32 v2, v200, v163, v208 bitop3:0x36
	v_lshl_add_u32 v10, v2, 4, v201
	s_waitcnt lgkmcnt(0)
	s_barrier
	ds_read_b128 v[2:5], v10 offset:24576
	ds_read_b128 v[6:9], v10 offset:32768
	ds_read_b128 v[86:89], v10 offset:8192
	ds_read_b128 v[82:85], v10 offset:16384
	s_waitcnt lgkmcnt(1)
	v_mfma_f32_32x32x16_bf16 v[18:33], v[2:5], v[86:89], 0
	v_bitop3_b32 v90, v200, v90, v208 bitop3:0x36
	v_lshl_add_u32 v90, v90, 4, v201
	ds_read_b128 v[98:101], v90 offset:24576
	ds_read_b128 v[102:105], v90 offset:32768
	ds_read_b128 v[94:97], v90 offset:8192
	ds_read_b128 v[90:93], v90 offset:16384
	s_waitcnt lgkmcnt(4)
	v_mfma_f32_32x32x16_bf16 v[34:49], v[2:5], v[82:85], 0
	v_mfma_f32_32x32x16_bf16 v[2:17], v[6:9], v[82:85], 0
	s_waitcnt lgkmcnt(1)
	v_mfma_f32_32x32x16_bf16 v[18:33], v[98:101], v[94:97], v[18:33]
	s_waitcnt lgkmcnt(0)
	v_mfma_f32_32x32x16_bf16 v[34:49], v[98:101], v[90:93], v[34:49]
	v_or_b32_e32 v98, 4, v163
	v_bitop3_b32 v98, v200, v98, v208 bitop3:0x36
	v_lshl_add_u32 v98, v98, 4, v201
	v_mfma_f32_32x32x16_bf16 v[2:17], v[102:105], v[90:93], v[2:17]
	ds_read_b128 v[106:109], v98 offset:24576
	ds_read_b128 v[110:113], v98 offset:32768
	ds_read_b128 v[102:105], v98 offset:8192
	ds_read_b128 v[98:101], v98 offset:16384
	s_waitcnt lgkmcnt(1)
	v_mfma_f32_32x32x16_bf16 v[18:33], v[106:109], v[102:105], v[18:33]
	s_waitcnt lgkmcnt(0)
	v_mfma_f32_32x32x16_bf16 v[34:49], v[106:109], v[98:101], v[34:49]
	v_or_b32_e32 v106, 6, v163
	v_bitop3_b32 v106, v200, v106, v208 bitop3:0x36
	v_lshl_add_u32 v106, v106, 4, v201
	v_mfma_f32_32x32x16_bf16 v[2:17], v[110:113], v[98:101], v[2:17]
	ds_read_b128 v[114:117], v106 offset:24576
	ds_read_b128 v[118:121], v106 offset:32768
	ds_read_b128 v[110:113], v106 offset:8192
	ds_read_b128 v[106:109], v106 offset:16384
	s_waitcnt lgkmcnt(1)
	v_mfma_f32_32x32x16_bf16 v[18:33], v[114:117], v[110:113], v[18:33]
	s_waitcnt lgkmcnt(0)
	v_mfma_f32_32x32x16_bf16 v[34:49], v[114:117], v[106:109], v[34:49]
	v_or_b32_e32 v114, 8, v163
	v_bitop3_b32 v114, v200, v114, v208 bitop3:0x36
	v_lshl_add_u32 v114, v114, 4, v201
	v_mfma_f32_32x32x16_bf16 v[2:17], v[118:121], v[106:109], v[2:17]
	ds_read_b128 v[122:125], v114 offset:24576
	ds_read_b128 v[126:129], v114 offset:32768
	ds_read_b128 v[118:121], v114 offset:8192
	ds_read_b128 v[114:117], v114 offset:16384
	s_waitcnt lgkmcnt(1)
	v_mfma_f32_32x32x16_bf16 v[18:33], v[122:125], v[118:121], v[18:33]
	s_waitcnt lgkmcnt(0)
	v_mfma_f32_32x32x16_bf16 v[34:49], v[122:125], v[114:117], v[34:49]
	v_or_b32_e32 v122, 10, v163
	v_bitop3_b32 v122, v200, v122, v208 bitop3:0x36
	v_lshl_add_u32 v122, v122, 4, v201
	v_mfma_f32_32x32x16_bf16 v[2:17], v[126:129], v[114:117], v[2:17]
	ds_read_b128 v[130:133], v122 offset:24576
	ds_read_b128 v[134:137], v122 offset:32768
	ds_read_b128 v[126:129], v122 offset:8192
	ds_read_b128 v[122:125], v122 offset:16384
	s_waitcnt lgkmcnt(1)
	v_mfma_f32_32x32x16_bf16 v[18:33], v[130:133], v[126:129], v[18:33]
	s_waitcnt lgkmcnt(0)
	v_mfma_f32_32x32x16_bf16 v[34:49], v[130:133], v[122:125], v[34:49]
	v_or_b32_e32 v130, 12, v163
	v_bitop3_b32 v130, v200, v130, v208 bitop3:0x36
	v_lshl_add_u32 v130, v130, 4, v201
	v_mfma_f32_32x32x16_bf16 v[2:17], v[134:137], v[122:125], v[2:17]
	ds_read_b128 v[138:141], v130 offset:24576
	ds_read_b128 v[142:145], v130 offset:32768
	ds_read_b128 v[134:137], v130 offset:8192
	ds_read_b128 v[130:133], v130 offset:16384
	s_waitcnt lgkmcnt(1)
	v_mfma_f32_32x32x16_bf16 v[18:33], v[138:141], v[134:137], v[18:33]
	s_waitcnt lgkmcnt(0)
	v_mfma_f32_32x32x16_bf16 v[34:49], v[138:141], v[130:133], v[34:49]
	v_or_b32_e32 v138, 14, v163
	v_bitop3_b32 v138, v200, v138, v208 bitop3:0x36
	v_mfma_f32_32x32x16_bf16 v[2:17], v[142:145], v[130:133], v[2:17]
	v_lshl_add_u32 v142, v138, 4, v201
	ds_read_b128 v[200:203], v142 offset:24576
	ds_read_b128 v[204:207], v142 offset:32768
	ds_read_b128 v[138:141], v142 offset:8192
	ds_read_b128 v[142:145], v142 offset:16384
	s_waitcnt lgkmcnt(1)
	v_mfma_f32_32x32x16_bf16 v[18:33], v[200:203], v[138:141], v[18:33]
	s_waitcnt lgkmcnt(0)
	v_mfma_f32_32x32x16_bf16 v[34:49], v[200:203], v[142:145], v[34:49]
	s_nop 9
	v_cndmask_b32_e64 v200, v18, 0, vcc
	v_cndmask_b32_e64 v18, v200, v18, s[46:47]
	v_or_b32_e32 v200, 2, v198
	v_cndmask_b32_e64 v19, 0, v19, s[46:47]
	v_cmp_le_u32_e64 s[46:47], v200, v197
	v_or_b32_e32 v200, 3, v198
	v_or_b32_e32 v201, 49, v198
	v_cndmask_b32_e64 v20, 0, v20, s[46:47]
	v_cmp_le_u32_e64 s[46:47], v200, v197
	v_or_b32_e32 v200, 8, v198
	v_mfma_f32_32x32x16_bf16 v[2:17], v[204:207], v[142:145], v[2:17]
	v_cndmask_b32_e64 v21, 0, v21, s[46:47]
	v_cmp_le_u32_e64 s[46:47], v200, v197
	v_or_b32_e32 v200, 9, v198
	v_or_b32_e32 v202, 50, v198
	v_cndmask_b32_e64 v22, 0, v22, s[46:47]
	v_cmp_le_u32_e64 s[46:47], v200, v197
	v_or_b32_e32 v200, 10, v198
	s_nop 4
	v_cndmask_b32_e64 v219, v2, 0, vcc
	v_cndmask_b32_e64 v23, 0, v23, s[46:47]
	v_cmp_le_u32_e64 s[46:47], v200, v197
	v_or_b32_e32 v200, 11, v198
	v_bfe_u32 v2, v161, 3, 3
	v_cndmask_b32_e64 v24, 0, v24, s[46:47]
	v_cmp_le_u32_e64 s[46:47], v200, v197
	v_or_b32_e32 v200, 16, v198
	v_or_b32_e32 v203, 51, v198
	v_cndmask_b32_e64 v25, 0, v25, s[46:47]
	v_cmp_le_u32_e64 s[46:47], v200, v197
	v_or_b32_e32 v200, 48, v198
	v_or_b32_e32 v204, 56, v198
	v_cndmask_b32_e64 v209, 0, v26, s[46:47]
	v_or_b32_e32 v26, 17, v198
	v_cmp_le_u32_e64 s[46:47], v26, v197
	v_or_b32_e32 v26, 18, v198
	v_or_b32_e32 v205, 57, v198
	v_cndmask_b32_e64 v212, 0, v27, s[46:47]
	v_cmp_le_u32_e64 s[46:47], v26, v197
	v_or_b32_e32 v26, 19, v198
	v_or_b32_e32 v27, 33, v198
	v_cndmask_b32_e64 v213, 0, v28, s[46:47]
	v_cmp_le_u32_e64 s[46:47], v26, v197
	v_or_b32_e32 v26, 24, v198
	v_or_b32_e32 v28, 34, v198
	v_cndmask_b32_e64 v214, 0, v29, s[46:47]
	v_cmp_le_u32_e64 s[46:47], v26, v197
	v_or_b32_e32 v26, 25, v198
	v_or_b32_e32 v29, 35, v198
	v_cndmask_b32_e64 v215, 0, v30, s[46:47]
	v_cmp_le_u32_e64 s[46:47], v26, v197
	v_or_b32_e32 v26, 26, v198
	v_or_b32_e32 v30, 40, v198
	v_cndmask_b32_e64 v216, 0, v31, s[46:47]
	v_cmp_le_u32_e64 s[46:47], v26, v197
	v_or_b32_e32 v26, 27, v198
	v_or_b32_e32 v31, 41, v198
	v_cndmask_b32_e64 v217, 0, v32, s[46:47]
	v_cmp_le_u32_e64 s[46:47], v26, v197
	v_or_b32_e32 v26, 32, v197
	v_cmp_le_u32_e32 vcc, v27, v26
	v_or_b32_e32 v32, 42, v198
	v_cndmask_b32_e64 v218, 0, v33, s[46:47]
	v_cndmask_b32_e32 v220, 0, v3, vcc
	v_cmp_le_u32_e32 vcc, v28, v26
	v_and_b32_e32 v3, 2, v2
	v_and_or_b32 v2, v2, 4, v208
	v_cndmask_b32_e32 v221, 0, v4, vcc
	v_lshrrev_b32_e32 v4, 1, v161
	v_cmp_le_u32_e32 vcc, v29, v26
	v_and_or_b32 v3, v4, 1, v3
	v_or_b32_e32 v4, s12, v3
	v_cndmask_b32_e32 v222, 0, v5, vcc
	v_cmp_le_u32_e32 vcc, v30, v26
	v_lshl_or_b32 v5, v208, 2, v163
	v_bitop3_b32 v3, v3, v5, s12 bitop3:0x36
	v_cndmask_b32_e32 v223, 0, v6, vcc
	v_cmp_le_u32_e32 vcc, v31, v26
	v_readlane_b32 s12, v253, 33
	v_lshlrev_b32_e32 v6, 3, v161
	v_bitop3_b32 v4, v5, v4, 2 bitop3:0x36
	v_cndmask_b32_e32 v224, 0, v7, vcc
	v_lshl_add_u32 v3, v3, 4, s12
	v_and_b32_e32 v6, 8, v6
	v_lshlrev_b32_e32 v7, 8, v2
	v_lshl_add_u32 v4, v4, 4, s12
	v_add3_u32 v161, v3, v6, v7
	v_add3_u32 v163, v4, v7, v6
	v_or_b32_e32 v33, 43, v198
	v_cmp_le_u32_e32 vcc, v32, v26
	ds_read_b64_tr_b16 v[2:3], v161 offset:40960
	ds_read_b64_tr_b16 v[4:5], v163 offset:43008
	v_cndmask_b32_e32 v225, 0, v8, vcc
	v_cmp_le_u32_e32 vcc, v33, v26
	v_or_b32_e32 v206, 58, v198
	v_or_b32_e32 v207, 59, v198
	v_cndmask_b32_e32 v226, 0, v9, vcc
	v_cmp_le_u32_e32 vcc, v200, v26
	v_cvt_pk_bf16_f32 v6, v18, v19
	v_cvt_pk_bf16_f32 v7, v20, v21
	v_cndmask_b32_e32 v200, 0, v10, vcc
	v_cmp_le_u32_e32 vcc, v201, v26
	v_cvt_pk_bf16_f32 v8, v22, v23
	v_cvt_pk_bf16_f32 v9, v24, v25
	v_cndmask_b32_e32 v201, 0, v11, vcc
	v_cmp_le_u32_e32 vcc, v202, v26
	s_add_i32 s12, s60, s70
	s_cmpk_gt_i32 s12, 0x3ff
	v_cndmask_b32_e32 v202, 0, v12, vcc
	v_cmp_le_u32_e32 vcc, v203, v26
	s_cselect_b64 s[46:47], -1, 0
	s_cmpk_lt_i32 s12, 0x400
	v_cndmask_b32_e32 v203, 0, v13, vcc
	v_cmp_le_u32_e32 vcc, v204, v26
	s_cselect_b32 s18, s12, s60
	s_ashr_i32 s20, s18, 8
	v_cndmask_b32_e32 v204, 0, v14, vcc
	v_cmp_le_u32_e32 vcc, v205, v26
	s_bfe_u32 s63, s18, 0x20006
	s_ashr_i32 s21, s20, 31
	v_cndmask_b32_e32 v205, 0, v15, vcc
	v_cmp_le_u32_e32 vcc, v206, v26
	s_lshl_b32 s18, s18, 6
	s_lshl_b64 s[20:21], s[20:21], 12
	v_cndmask_b32_e32 v206, 0, v16, vcc
	v_cmp_le_u32_e32 vcc, v207, v26
	s_waitcnt lgkmcnt(0)
	v_mfma_f32_32x32x16_bf16 v[18:33], v[2:5], v[6:9], 0
	v_cvt_pk_bf16_f32 v6, v34, v35
	v_cvt_pk_bf16_f32 v7, v36, v37
	v_cvt_pk_bf16_f32 v8, v38, v39
	v_cvt_pk_bf16_f32 v9, v40, v41
	v_cndmask_b32_e32 v207, 0, v17, vcc
	ds_read_b64_tr_b16 v[34:35], v161 offset:45056
	ds_read_b64_tr_b16 v[36:37], v163 offset:47104
	v_cvt_pk_bf16_f32 v38, v209, v212
	v_mfma_f32_32x32x16_bf16 v[2:17], v[2:5], v[6:9], 0
	v_cvt_pk_bf16_f32 v39, v213, v214
	v_cvt_pk_bf16_f32 v40, v215, v216
	v_cvt_pk_bf16_f32 v41, v217, v218
	s_and_b32 s18, s18, 0xfc0
	s_or_b32 s20, s20, s18
	s_lshl_b32 s30, s63, 8
	v_readlane_b32 s18, v253, 45
	s_waitcnt lgkmcnt(0)
	v_mfma_f32_32x32x16_bf16 v[18:33], v[34:37], v[38:41], v[18:33]
	v_cvt_pk_bf16_f32 v38, v42, v43
	v_cvt_pk_bf16_f32 v39, v44, v45
	v_cvt_pk_bf16_f32 v40, v46, v47
	v_cvt_pk_bf16_f32 v41, v48, v49
	v_cvt_pk_bf16_f32 v42, v219, v220
	v_cvt_pk_bf16_f32 v43, v221, v222
	v_cvt_pk_bf16_f32 v44, v223, v224
	v_mfma_f32_32x32x16_bf16 v[2:17], v[34:37], v[38:41], v[2:17]
	ds_read_b64_tr_b16 v[34:35], v161 offset:49152
	ds_read_b64_tr_b16 v[36:37], v163 offset:51200
	v_mov_b64_e32 v[38:39], s[64:65]
	v_mov_b64_e32 v[40:41], s[66:67]
	v_cvt_pk_bf16_f32 v45, v225, v226
	v_add_u32_e32 v0, s18, v0
	s_waitcnt lgkmcnt(0)
	v_mfma_f32_32x32x16_bf16 v[18:33], v[34:37], v[38:41], v[18:33]
	v_mfma_f32_32x32x16_bf16 v[2:17], v[34:37], v[42:45], v[2:17]
	ds_read_b64_tr_b16 v[34:35], v161 offset:53248
	ds_read_b64_tr_b16 v[36:37], v163 offset:55296
	v_lshl_add_u64 v[42:43], s[20:21], 0, v[148:149]
	v_mov_b32_e32 v161, v1
	v_mad_u64_u32 v[44:45], s[60:61], v42, s72, v[180:181]
	v_mad_i32_i24 v45, v43, s72, v45
	v_lshl_add_u64 v[42:43], v[44:45], 0, s[30:31]
	s_waitcnt lgkmcnt(0)
	v_mfma_f32_32x32x16_bf16 v[18:33], v[34:37], v[38:41], v[18:33]
	v_cvt_pk_bf16_f32 v38, v200, v201
	v_cvt_pk_bf16_f32 v39, v202, v203
	v_cvt_pk_bf16_f32 v40, v204, v205
	v_cvt_pk_bf16_f32 v41, v206, v207
	v_lshl_add_u64 v[42:43], v[42:43], 0, v[160:161]
	v_mov_b32_e32 v163, v1
	v_mfma_f32_32x32x16_bf16 v[2:17], v[34:37], v[38:41], v[2:17]
	v_lshl_add_u64 v[34:35], s[20:21], 0, v[146:147]
	v_mad_u64_u32 v[36:37], s[60:61], v34, s72, v[180:181]
	v_mad_i32_i24 v37, v35, s72, v37
	v_lshl_add_u64 v[34:35], v[36:37], 0, s[30:31]
	v_lshl_add_u64 v[34:35], v[34:35], 0, v[160:161]
	v_add_co_u32_e32 v38, vcc, s68, v34
	v_mfma_f32_32x32x16_bf16 v[18:33], v[78:81], v[86:89], v[18:33]
	s_nop 0
	v_addc_co_u32_e32 v39, vcc, 0, v35, vcc
	s_lshl_b32 s30, s63, 9
	v_add_co_u32_e32 v46, vcc, s68, v42
	s_nop 1
	v_addc_co_u32_e32 v47, vcc, 0, v43, vcc
	v_mfma_f32_32x32x16_bf16 v[2:17], v[78:81], v[82:85], v[2:17]
	v_mfma_f32_32x32x16_bf16 v[18:33], v[74:77], v[94:97], v[18:33]
	v_mfma_f32_32x32x16_bf16 v[2:17], v[74:77], v[90:93], v[2:17]
	v_mfma_f32_32x32x16_bf16 v[18:33], v[70:73], v[102:105], v[18:33]
	v_mfma_f32_32x32x16_bf16 v[2:17], v[70:73], v[98:101], v[2:17]
	v_mfma_f32_32x32x16_bf16 v[18:33], v[66:69], v[110:113], v[18:33]
	v_mfma_f32_32x32x16_bf16 v[2:17], v[66:69], v[106:109], v[2:17]
	v_lshl_add_u64 v[66:67], s[20:21], 0, v[150:151]
	v_mad_u64_u32 v[68:69], s[60:61], v66, s72, v[180:181]
	v_mad_i32_i24 v69, v67, s72, v69
	v_lshl_add_u64 v[66:67], v[68:69], 0, s[30:31]
	v_lshl_add_u64 v[66:67], v[66:67], 0, v[162:163]
	v_add_co_u32_e32 v66, vcc, s69, v66
	v_mfma_f32_32x32x16_bf16 v[18:33], v[62:65], v[118:121], v[18:33]
	s_nop 0
	v_addc_co_u32_e32 v67, vcc, 0, v67, vcc
	v_mfma_f32_32x32x16_bf16 v[2:17], v[62:65], v[114:117], v[2:17]
	v_mfma_f32_32x32x16_bf16 v[18:33], v[58:61], v[126:129], v[18:33]
	v_mfma_f32_32x32x16_bf16 v[2:17], v[58:61], v[122:125], v[2:17]
	v_mfma_f32_32x32x16_bf16 v[18:33], v[54:57], v[134:137], v[18:33]
	v_mfma_f32_32x32x16_bf16 v[2:17], v[54:57], v[130:133], v[2:17]
	v_mfma_f32_32x32x16_bf16 v[18:33], v[50:53], v[138:141], v[18:33]
	v_mfma_f32_32x32x16_bf16 v[2:17], v[50:53], v[142:145], v[2:17]
	global_load_dwordx4 v[62:65], v182, s[58:59]
	global_load_dwordx4 v[58:61], v182, s[58:59] offset:32
	global_load_dwordx4 v[54:57], v182, s[58:59] offset:64
	global_load_dwordx4 v[50:53], v182, s[58:59] offset:96
	global_load_dwordx4 v[34:37], v[38:39], off offset:2048
	s_nop 0
	global_load_dwordx4 v[38:41], v[38:39], off offset:3072
	s_nop 0
	global_load_dwordx4 v[42:45], v[46:47], off offset:2048
	s_nop 0
	global_load_dwordx4 v[46:49], v[46:47], off offset:3072
	s_nop 0
	global_load_dwordx4 v[82:85], v[66:67], off
	v_lshl_add_u64 v[66:67], s[20:21], 0, v[152:153]
	v_mad_u64_u32 v[68:69], s[60:61], v66, s72, v[180:181]
	v_mad_i32_i24 v69, v67, s72, v69
	v_lshl_add_u64 v[66:67], v[68:69], 0, s[30:31]
	v_lshl_add_u64 v[66:67], v[66:67], 0, v[162:163]
	v_add_co_u32_e32 v66, vcc, s69, v66
	s_nop 1
	v_addc_co_u32_e32 v67, vcc, 0, v67, vcc
	global_load_dwordx4 v[86:89], v[66:67], off
	v_lshl_add_u64 v[66:67], s[20:21], 0, v[154:155]
	v_mad_u64_u32 v[68:69], s[60:61], v66, s72, v[180:181]
	v_mad_i32_i24 v69, v67, s72, v69
	v_lshl_add_u64 v[66:67], v[68:69], 0, s[30:31]
	v_lshl_add_u64 v[66:67], v[66:67], 0, v[162:163]
	v_add_co_u32_e32 v66, vcc, s69, v66
	s_nop 1
	v_addc_co_u32_e32 v67, vcc, 0, v67, vcc
	global_load_dwordx4 v[90:93], v[66:67], off
	v_lshl_add_u64 v[66:67], s[20:21], 0, v[156:157]
	v_mad_u64_u32 v[68:69], s[20:21], v66, s72, v[180:181]
	v_mad_i32_i24 v69, v67, s72, v69
	v_lshl_add_u64 v[66:67], v[68:69], 0, s[30:31]
	v_lshl_add_u64 v[66:67], v[66:67], 0, v[162:163]
	v_add_co_u32_e32 v66, vcc, s69, v66
	s_nop 1
	v_addc_co_u32_e32 v67, vcc, 0, v67, vcc
	global_load_dwordx4 v[94:97], v[66:67], off
	v_mul_f32_e32 v66, v19, v19
	v_fmac_f32_e32 v66, v18, v18
	v_fmac_f32_e32 v66, v20, v20
	v_fmac_f32_e32 v66, v21, v21
	v_fmac_f32_e32 v66, v22, v22
	v_fmac_f32_e32 v66, v23, v23
	v_fmac_f32_e32 v66, v24, v24
	v_fmac_f32_e32 v66, v25, v25
	v_fmac_f32_e32 v66, v26, v26
	v_fmac_f32_e32 v66, v27, v27
	v_fmac_f32_e32 v66, v28, v28
	v_fmac_f32_e32 v66, v29, v29
	v_fmac_f32_e32 v66, v30, v30
	v_fmac_f32_e32 v66, v31, v31
	v_fmac_f32_e32 v66, v32, v32
	v_fmac_f32_e32 v66, v33, v33
	v_mov_b32_e32 v67, v66
	v_cmp_gt_u32_e32 vcc, 32, v199
	s_nop 0
	v_permlane32_swap_b32_e32 v66, v67
	s_and_saveexec_b64 s[60:61], vcc
	v_add_f32_e32 v66, v66, v67
	ds_write_b32 v0, v66 offset:6144
	s_or_b64 exec, exec, s[60:61]
	v_mul_f32_e32 v66, v3, v3
	v_fmac_f32_e32 v66, v2, v2
	v_fmac_f32_e32 v66, v4, v4
	v_fmac_f32_e32 v66, v5, v5
	v_fmac_f32_e32 v66, v6, v6
	v_fmac_f32_e32 v66, v7, v7
	v_fmac_f32_e32 v66, v8, v8
	v_fmac_f32_e32 v66, v9, v9
	v_fmac_f32_e32 v66, v10, v10
	v_fmac_f32_e32 v66, v11, v11
	v_fmac_f32_e32 v66, v12, v12
	v_fmac_f32_e32 v66, v13, v13
	v_fmac_f32_e32 v66, v14, v14
	v_fmac_f32_e32 v66, v15, v15
	v_fmac_f32_e32 v66, v16, v16
	v_fmac_f32_e32 v66, v17, v17
	v_mov_b32_e32 v67, v66
	s_nop 1
	v_permlane32_swap_b32_e32 v66, v67
	s_and_saveexec_b64 s[60:61], vcc
	s_cbranch_execz .LBB0_521
	v_add_f32_e32 v66, v66, v67
	ds_write_b32 v0, v66 offset:6272
	s_branch .LBB0_521
